# attention main loop: forget-bias add for the next tile moved from the step head to just before the step barrier
# baseline (speedup 1.0000x reference)
.LBB0_727:
	v_mfma_f32_32x32x16_bf16 v[16:31], v[126:129], v[190:193], v[16:31]
	v_exp_f32_e32 v48, v48
	v_exp_f32_e32 v49, v49
	v_exp_f32_e32 v50, v50
	v_exp_f32_e32 v51, v51
	s_waitcnt lgkmcnt(14)
	v_mfma_f32_32x32x16_bf16 v[0:15], v[126:129], v[186:189], v[0:15]
	v_exp_f32_e32 v52, v52
	v_exp_f32_e32 v53, v53
	v_exp_f32_e32 v54, v54
	v_exp_f32_e32 v55, v55
	v_add_u32_e32 v80, s22, v238
	ds_read_b128 v[134:137], v80
	ds_read_b128 v[130:133], v80 offset:512
	v_mfma_f32_32x32x16_bf16 v[16:31], v[122:125], v[182:185], v[16:31]
	v_exp_f32_e32 v56, v56
	v_exp_f32_e32 v57, v57
	v_exp_f32_e32 v58, v58
	v_exp_f32_e32 v59, v59
	ds_read_b128 v[146:149], v80 offset:2048
	ds_read_b128 v[142:145], v80 offset:2560
	v_mfma_f32_32x32x16_bf16 v[0:15], v[122:125], v[178:181], v[0:15]
	v_exp_f32_e32 v60, v60
	v_exp_f32_e32 v61, v61
	v_exp_f32_e32 v62, v62
	v_exp_f32_e32 v63, v63
	ds_read_b128 v[158:161], v80 offset:4096
	ds_read_b128 v[154:157], v80 offset:4608
	v_mfma_f32_32x32x16_bf16 v[16:31], v[118:121], v[166:169], v[16:31]
	v_exp_f32_e32 v32, v32
	v_exp_f32_e32 v33, v33
	v_exp_f32_e32 v34, v34
	v_exp_f32_e32 v35, v35
	ds_read_b128 v[166:169], v80 offset:6144
	ds_read_b128 v[150:153], v80 offset:6656
	s_waitcnt lgkmcnt(14)
	v_mfma_f32_32x32x16_bf16 v[0:15], v[118:121], v[174:177], v[0:15]
	v_exp_f32_e32 v36, v36
	v_exp_f32_e32 v37, v37
	v_exp_f32_e32 v38, v38
	v_exp_f32_e32 v39, v39
	v_mfma_f32_32x32x16_bf16 v[16:31], v[114:117], v[170:173], v[16:31]
	v_exp_f32_e32 v40, v40
	v_exp_f32_e32 v41, v41
	v_exp_f32_e32 v42, v42
	v_exp_f32_e32 v43, v43
	v_mfma_f32_32x32x16_bf16 v[0:15], v[114:117], v[162:165], v[0:15]
	v_exp_f32_e32 v44, v44
	v_exp_f32_e32 v45, v45
	v_exp_f32_e32 v46, v46
	v_exp_f32_e32 v47, v47
	s_waitcnt vmcnt(2) lgkmcnt(0)
	v_pk_add_f32 v[80:81], v[64:65], v[202:203] op_sel_hi:[1,0] neg_lo:[0,1] neg_hi:[0,1]
	v_pk_add_f32 v[64:65], v[82:83], v[202:203] op_sel_hi:[1,0] neg_lo:[0,1] neg_hi:[0,1]
	v_pk_add_f32 v[82:83], v[66:67], v[202:203] op_sel_hi:[1,0] neg_lo:[0,1] neg_hi:[0,1]
	v_pk_add_f32 v[66:67], v[84:85], v[202:203] op_sel_hi:[1,0] neg_lo:[0,1] neg_hi:[0,1]
	v_pk_add_f32 v[84:85], v[68:69], v[202:203] op_sel_hi:[1,0] neg_lo:[0,1] neg_hi:[0,1]
	v_pk_add_f32 v[68:69], v[86:87], v[202:203] op_sel_hi:[1,0] neg_lo:[0,1] neg_hi:[0,1]
	v_pk_add_f32 v[86:87], v[70:71], v[202:203] op_sel_hi:[1,0] neg_lo:[0,1] neg_hi:[0,1]
	v_pk_add_f32 v[70:71], v[88:89], v[202:203] op_sel_hi:[1,0] neg_lo:[0,1] neg_hi:[0,1]
	v_pk_add_f32 v[88:89], v[72:73], v[202:203] op_sel_hi:[1,0] neg_lo:[0,1] neg_hi:[0,1]
	v_pk_add_f32 v[72:73], v[90:91], v[202:203] op_sel_hi:[1,0] neg_lo:[0,1] neg_hi:[0,1]
	v_pk_add_f32 v[90:91], v[74:75], v[202:203] op_sel_hi:[1,0] neg_lo:[0,1] neg_hi:[0,1]
	v_pk_add_f32 v[74:75], v[92:93], v[202:203] op_sel_hi:[1,0] neg_lo:[0,1] neg_hi:[0,1]
	v_pk_add_f32 v[92:93], v[76:77], v[202:203] op_sel_hi:[1,0] neg_lo:[0,1] neg_hi:[0,1]
	v_pk_add_f32 v[76:77], v[138:139], v[202:203] op_sel_hi:[1,0] neg_lo:[0,1] neg_hi:[0,1]
	v_pk_add_f32 v[94:95], v[78:79], v[202:203] op_sel_hi:[1,0] neg_lo:[0,1] neg_hi:[0,1]
	v_pk_add_f32 v[78:79], v[140:141], v[202:203] op_sel_hi:[1,0] neg_lo:[0,1] neg_hi:[0,1]
	s_barrier
	s_andn2_b64 vcc, exec, s[18:19]
	s_cbranch_vccnz .LBB0_729
	s_waitcnt lgkmcnt(0)
	ds_read_b128 v[162:165], v219 offset:49248
	ds_read_b128 v[170:173], v219 offset:49216
	ds_read_b128 v[174:177], v219 offset:49184
	ds_read_b128 v[178:181], v219 offset:49152
	s_waitcnt lgkmcnt(3)
	v_pk_mul_f32 v[30:31], v[30:31], v[164:165]
	s_waitcnt lgkmcnt(2)
	v_pk_mul_f32 v[26:27], v[26:27], v[172:173]
	s_waitcnt lgkmcnt(1)
	v_pk_mul_f32 v[22:23], v[22:23], v[176:177]
	s_waitcnt lgkmcnt(0)
	v_pk_mul_f32 v[18:19], v[18:19], v[180:181]
	v_pk_mul_f32 v[28:29], v[28:29], v[162:163]
	v_pk_mul_f32 v[24:25], v[24:25], v[170:171]
	v_pk_mul_f32 v[20:21], v[20:21], v[174:175]
	v_pk_mul_f32 v[16:17], v[16:17], v[178:179]
	v_pk_mul_f32 v[14:15], v[14:15], v[164:165]
	v_pk_mul_f32 v[10:11], v[10:11], v[172:173]
	v_pk_mul_f32 v[6:7], v[6:7], v[176:177]
	v_pk_mul_f32 v[2:3], v[2:3], v[180:181]
	v_pk_mul_f32 v[12:13], v[12:13], v[162:163]
	v_pk_mul_f32 v[8:9], v[8:9], v[170:171]
	v_pk_mul_f32 v[4:5], v[4:5], v[174:175]
	v_pk_mul_f32 v[0:1], v[0:1], v[178:179]
.LBB0_729:
	s_add_i32 s18, s22, 0x2000
	v_add_u32_e32 v162, s38, v239
	s_cmpk_lg_i32 s22, 0x4000
	s_cselect_b32 s38, s18, 0
	s_add_i32 s18, s22, s30
	s_mov_b32 s19, m0
	s_mov_b32 m0, s18
	s_nop 0
	global_load_lds_dwordx4 v244, s[98:99]
	s_mov_b32 m0, s19
	s_add_i32 s18, s38, s31
	s_mov_b32 s19, m0
	s_mov_b32 m0, s18
	s_nop 0
	global_load_lds_dwordx4 v245, s[98:99]
	s_mov_b32 m0, s19
	s_add_u32 s98, s98, 0x20000
	s_addc_u32 s99, s99, 0
	ds_read_b64_tr_b16 v[194:195], v162 offset:24576
	ds_read_b64_tr_b16 v[196:197], v162 offset:25088
	s_waitcnt lgkmcnt(2)
	v_mfma_f32_32x32x16_bf16 v[80:95], v[134:137], v[110:113], v[80:95]
	v_add_f32_e32 v114, v48, v49
	v_add_f32_e32 v114, v50, v114
	v_add_f32_e32 v114, v51, v114
	v_add_f32_e32 v114, v52, v114
	v_add_f32_e32 v114, v53, v114
	v_cvt_pk_bf16_f32 v126, v48, v49
	v_cvt_pk_bf16_f32 v127, v50, v51
	ds_read_b64_tr_b16 v[190:191], v162 offset:28672
	ds_read_b64_tr_b16 v[192:193], v162 offset:29184
	v_mfma_f32_32x32x16_bf16 v[64:79], v[130:133], v[110:113], v[64:79]
	v_add_f32_e32 v48, v54, v114
	v_add_f32_e32 v48, v55, v48
	v_add_f32_e32 v48, v56, v48
	v_add_f32_e32 v48, v57, v48
	v_cvt_pk_bf16_f32 v128, v52, v53
	v_cvt_pk_bf16_f32 v129, v54, v55
	ds_read_b64_tr_b16 v[186:187], v162 offset:25600
	ds_read_b64_tr_b16 v[188:189], v162 offset:26112
	v_mfma_f32_32x32x16_bf16 v[80:95], v[146:149], v[106:109], v[80:95]
	v_add_f32_e32 v48, v58, v48
	v_add_f32_e32 v48, v59, v48
	v_add_f32_e32 v48, v60, v48
	v_add_f32_e32 v48, v61, v48
	v_cvt_pk_bf16_f32 v122, v56, v57
	v_cvt_pk_bf16_f32 v123, v58, v59
	ds_read_b64_tr_b16 v[138:139], v162 offset:29696
	ds_read_b64_tr_b16 v[140:141], v162 offset:30208
	v_mfma_f32_32x32x16_bf16 v[64:79], v[142:145], v[106:109], v[64:79]
	v_add_f32_e32 v48, v62, v48
	v_add_f32_e32 v48, v63, v48
	v_add_f32_e32 v48, v32, v48
	v_add_f32_e32 v48, v33, v48
	v_cvt_pk_bf16_f32 v124, v60, v61
	v_cvt_pk_bf16_f32 v125, v62, v63
	ds_read_b64_tr_b16 v[182:183], v162 offset:26624
	ds_read_b64_tr_b16 v[184:185], v162 offset:27136
	v_mfma_f32_32x32x16_bf16 v[80:95], v[158:161], v[102:105], v[80:95]
	v_add_f32_e32 v48, v34, v48
	v_add_f32_e32 v48, v35, v48
	v_add_f32_e32 v48, v36, v48
	v_add_f32_e32 v48, v37, v48
	v_cvt_pk_bf16_f32 v118, v32, v33
	v_cvt_pk_bf16_f32 v119, v34, v35
	ds_read_b64_tr_b16 v[178:179], v162 offset:30720
	ds_read_b64_tr_b16 v[180:181], v162 offset:31232
	v_mfma_f32_32x32x16_bf16 v[64:79], v[154:157], v[102:105], v[64:79]
	v_add_f32_e32 v32, v38, v48
	v_add_f32_e32 v32, v39, v32
	v_add_f32_e32 v32, v40, v32
	v_add_f32_e32 v32, v41, v32
	v_cvt_pk_bf16_f32 v120, v36, v37
	v_cvt_pk_bf16_f32 v121, v38, v39
	ds_read_b64_tr_b16 v[174:175], v162 offset:27648
	ds_read_b64_tr_b16 v[176:177], v162 offset:28160
	v_mfma_f32_32x32x16_bf16 v[80:95], v[166:169], v[98:101], v[80:95]
	v_add_f32_e32 v32, v42, v32
	v_add_f32_e32 v32, v43, v32
	v_add_f32_e32 v32, v44, v32
	v_add_f32_e32 v32, v45, v32
	v_cvt_pk_bf16_f32 v114, v40, v41
	v_cvt_pk_bf16_f32 v115, v42, v43
	ds_read_b64_tr_b16 v[170:171], v162 offset:31744
	ds_read_b64_tr_b16 v[172:173], v162 offset:32256
	v_mfma_f32_32x32x16_bf16 v[64:79], v[150:153], v[98:101], v[64:79]
	v_add_f32_e32 v32, v46, v32
	v_add_f32_e32 v32, v47, v32
	v_add_f32_e32 v240, v224, v32
	v_cvt_pk_bf16_f32 v116, v44, v45
	v_cvt_pk_bf16_f32 v117, v46, v47
	s_waitcnt lgkmcnt(14)
	ds_read_b128 v[32:35], v205 offset:256
	ds_read_b128 v[36:39], v205 offset:288
	ds_read_b128 v[50:53], v205 offset:384
	ds_read_b128 v[54:57], v205 offset:416
	ds_read_b128 v[40:43], v205 offset:320
	ds_read_b128 v[44:47], v205 offset:352
	ds_read_b128 v[58:61], v205 offset:448
	ds_read_b128 v[162:165], v205 offset:480
	v_max_f32_e32 v48, v80, v81
	v_max3_f32 v49, v82, v83, v65
	v_max3_f32 v48, v48, v64, v66
	v_max3_f32 v48, v48, v67, v84
	v_max3_f32 v49, v49, v86, v87
	v_max3_f32 v48, v48, v85, v68
	v_max3_f32 v49, v49, v70, v71
	v_max3_f32 v48, v48, v69, v88
	v_max3_f32 v49, v49, v90, v91
	v_max3_f32 v48, v48, v89, v72
	v_max3_f32 v49, v49, v74, v75
	v_max3_f32 v48, v48, v73, v92
	v_max3_f32 v49, v49, v94, v95
	v_max3_f32 v48, v48, v93, v76
	v_max3_f32 v49, v49, v78, v79
	v_max3_f32 v48, v48, v77, v49
	v_mov_b32_e32 v49, v48
	s_nop 1
	v_permlane32_swap_b32_e32 v48, v49
	v_max_f32_e32 v48, v48, v49
	v_cmp_lt_f32_e32 vcc, s51, v48
	s_cmp_lg_u64 vcc, 0
	s_cselect_b64 s[18:19], -1, 0
	s_cbranch_vccnz .LBB0_737
.LBB0_730:
	v_mfma_f32_32x32x16_bf16 v[16:31], v[126:129], v[194:197], v[16:31]
	v_exp_f32_e32 v80, v80
	v_exp_f32_e32 v81, v81
	v_exp_f32_e32 v82, v82
	v_exp_f32_e32 v83, v83
	s_waitcnt lgkmcnt(14)
	v_mfma_f32_32x32x16_bf16 v[0:15], v[126:129], v[190:193], v[0:15]
	v_exp_f32_e32 v84, v84
	v_exp_f32_e32 v85, v85
	v_exp_f32_e32 v86, v86
	v_exp_f32_e32 v87, v87
	v_add_u32_e32 v48, s38, v238
	ds_read_b128 v[158:161], v48
	ds_read_b128 v[146:149], v48 offset:512
	v_mfma_f32_32x32x16_bf16 v[16:31], v[122:125], v[186:189], v[16:31]
	v_exp_f32_e32 v88, v88
	v_exp_f32_e32 v89, v89
	v_exp_f32_e32 v90, v90
	v_exp_f32_e32 v91, v91
	ds_read_b128 v[154:157], v48 offset:2048
	ds_read_b128 v[142:145], v48 offset:2560
	v_mfma_f32_32x32x16_bf16 v[0:15], v[122:125], v[138:141], v[0:15]
	v_exp_f32_e32 v92, v92
	v_exp_f32_e32 v93, v93
	v_exp_f32_e32 v94, v94
	v_exp_f32_e32 v95, v95
	ds_read_b128 v[150:153], v48 offset:4096
	ds_read_b128 v[138:141], v48 offset:4608
	v_mfma_f32_32x32x16_bf16 v[16:31], v[118:121], v[182:185], v[16:31]
	v_exp_f32_e32 v64, v64
	v_exp_f32_e32 v65, v65
	v_exp_f32_e32 v66, v66
	v_exp_f32_e32 v67, v67
	ds_read_b128 v[134:137], v48 offset:6144
	ds_read_b128 v[130:133], v48 offset:6656
	s_waitcnt lgkmcnt(14)
	v_mfma_f32_32x32x16_bf16 v[0:15], v[118:121], v[178:181], v[0:15]
	v_exp_f32_e32 v68, v68
	v_exp_f32_e32 v69, v69
	v_exp_f32_e32 v70, v70
	v_exp_f32_e32 v71, v71
	v_mfma_f32_32x32x16_bf16 v[16:31], v[114:117], v[174:177], v[16:31]
	v_exp_f32_e32 v72, v72
	v_exp_f32_e32 v73, v73
	v_exp_f32_e32 v74, v74
	v_exp_f32_e32 v75, v75
	v_mfma_f32_32x32x16_bf16 v[0:15], v[114:117], v[170:173], v[0:15]
	v_exp_f32_e32 v76, v76
	v_exp_f32_e32 v77, v77
	v_exp_f32_e32 v78, v78
	v_exp_f32_e32 v79, v79
	s_waitcnt vmcnt(2) lgkmcnt(0)
	v_pk_add_f32 v[48:49], v[32:33], v[202:203] op_sel_hi:[1,0] neg_lo:[0,1] neg_hi:[0,1]
	v_pk_add_f32 v[32:33], v[50:51], v[202:203] op_sel_hi:[1,0] neg_lo:[0,1] neg_hi:[0,1]
	v_pk_add_f32 v[50:51], v[34:35], v[202:203] op_sel_hi:[1,0] neg_lo:[0,1] neg_hi:[0,1]
	v_pk_add_f32 v[34:35], v[52:53], v[202:203] op_sel_hi:[1,0] neg_lo:[0,1] neg_hi:[0,1]
	v_pk_add_f32 v[52:53], v[36:37], v[202:203] op_sel_hi:[1,0] neg_lo:[0,1] neg_hi:[0,1]
	v_pk_add_f32 v[36:37], v[54:55], v[202:203] op_sel_hi:[1,0] neg_lo:[0,1] neg_hi:[0,1]
	v_pk_add_f32 v[54:55], v[38:39], v[202:203] op_sel_hi:[1,0] neg_lo:[0,1] neg_hi:[0,1]
	v_pk_add_f32 v[38:39], v[56:57], v[202:203] op_sel_hi:[1,0] neg_lo:[0,1] neg_hi:[0,1]
	v_pk_add_f32 v[56:57], v[40:41], v[202:203] op_sel_hi:[1,0] neg_lo:[0,1] neg_hi:[0,1]
	v_pk_add_f32 v[40:41], v[58:59], v[202:203] op_sel_hi:[1,0] neg_lo:[0,1] neg_hi:[0,1]
	v_pk_add_f32 v[58:59], v[42:43], v[202:203] op_sel_hi:[1,0] neg_lo:[0,1] neg_hi:[0,1]
	v_pk_add_f32 v[42:43], v[60:61], v[202:203] op_sel_hi:[1,0] neg_lo:[0,1] neg_hi:[0,1]
	v_pk_add_f32 v[60:61], v[44:45], v[202:203] op_sel_hi:[1,0] neg_lo:[0,1] neg_hi:[0,1]
	v_pk_add_f32 v[44:45], v[162:163], v[202:203] op_sel_hi:[1,0] neg_lo:[0,1] neg_hi:[0,1]
	v_pk_add_f32 v[62:63], v[46:47], v[202:203] op_sel_hi:[1,0] neg_lo:[0,1] neg_hi:[0,1]
	v_pk_add_f32 v[46:47], v[164:165], v[202:203] op_sel_hi:[1,0] neg_lo:[0,1] neg_hi:[0,1]
	s_barrier
	s_andn2_b64 vcc, exec, s[18:19]
	s_cbranch_vccnz .LBB0_732
	s_waitcnt lgkmcnt(0)
	ds_read_b128 v[166:169], v219 offset:49248
	ds_read_b128 v[170:173], v219 offset:49216
	ds_read_b128 v[174:177], v219 offset:49184
	ds_read_b128 v[178:181], v219 offset:49152
	s_waitcnt lgkmcnt(3)
	v_pk_mul_f32 v[30:31], v[30:31], v[168:169]
	s_waitcnt lgkmcnt(2)
	v_pk_mul_f32 v[26:27], v[26:27], v[172:173]
	s_waitcnt lgkmcnt(1)
	v_pk_mul_f32 v[22:23], v[22:23], v[176:177]
	s_waitcnt lgkmcnt(0)
	v_pk_mul_f32 v[18:19], v[18:19], v[180:181]
	v_pk_mul_f32 v[28:29], v[28:29], v[166:167]
	v_pk_mul_f32 v[24:25], v[24:25], v[170:171]
	v_pk_mul_f32 v[20:21], v[20:21], v[174:175]
	v_pk_mul_f32 v[16:17], v[16:17], v[178:179]
	v_pk_mul_f32 v[14:15], v[14:15], v[168:169]
	v_pk_mul_f32 v[10:11], v[10:11], v[172:173]
	v_pk_mul_f32 v[6:7], v[6:7], v[176:177]
	v_pk_mul_f32 v[2:3], v[2:3], v[180:181]
	v_pk_mul_f32 v[12:13], v[12:13], v[166:167]
	v_pk_mul_f32 v[8:9], v[8:9], v[170:171]
	v_pk_mul_f32 v[4:5], v[4:5], v[174:175]
	v_pk_mul_f32 v[0:1], v[0:1], v[178:179]
.LBB0_732:
	s_add_i32 s18, s38, 0x2000
	s_cmpk_lg_i32 s38, 0x4000
	s_cselect_b32 s46, s18, 0
	s_add_i32 s18, s23, 2
	s_mov_b64 s[20:21], 0x40000
	v_lshl_add_u64 v[206:207], v[206:207], 0, s[20:21]
	s_mov_b64 s[62:63], 0x40000
	v_lshl_add_u64 v[208:209], v[208:209], 0, s[20:21]
	s_cmp_ge_u32 s18, s39
	v_add_u32_e32 v205, 0x200, v205
	s_cbranch_scc1 .LBB0_749
	s_mov_b32 s23, s18
	s_mov_b32 s18, s22
	s_mov_b32 s22, s46
	s_branch .LBB0_726
